# baseline (speedup 1.0000x reference)
.Lm_after0:
.Lm_steps1:
	s_waitcnt lgkmcnt(4)
	v_mfma_f32_32x32x16_f16 v[48:63], v[88:91], v[8:11], 0
	ds_read_b128 v[92:95], v128 offset:27648
	ds_read_b128 v[96:99], v128 offset:8192
	ds_read_b128 v[104:107], v128 offset:10240
	v_exp_f32_e32 v64, v64
	v_exp_f32_e32 v65, v65
	v_exp_f32_e32 v66, v66
	v_exp_f32_e32 v67, v67
	v_mfma_f32_32x32x16_bf16 v[16:31], v[100:103], v[84:87], v[16:31]
	v_exp_f32_e32 v68, v68
	v_exp_f32_e32 v69, v69
	v_exp_f32_e32 v70, v70
	v_exp_f32_e32 v71, v71
	v_mfma_f32_32x32x16_bf16 v[32:47], v[108:111], v[84:87], v[32:47]
	v_cvt_pk_bf16_f32 v80, v64, v65
	v_cvt_pk_bf16_f32 v81, v66, v67
	v_cvt_pk_bf16_f32 v82, v68, v69
	v_cvt_pk_bf16_f32 v83, v70, v71
	ds_read_b128 v[100:103], v128 offset:9216
	ds_read_b128 v[108:111], v128 offset:11264
	v_exp_f32_e32 v72, v72
	v_exp_f32_e32 v73, v73
	v_exp_f32_e32 v74, v74
	v_exp_f32_e32 v75, v75
	s_waitcnt lgkmcnt(7)
	v_mfma_f32_32x32x16_bf16 v[16:31], v[112:115], v[80:83], v[16:31]
	v_exp_f32_e32 v76, v76
	v_exp_f32_e32 v77, v77
	v_exp_f32_e32 v78, v78
	v_exp_f32_e32 v79, v79
	v_mfma_f32_32x32x16_bf16 v[32:47], v[120:123], v[80:83], v[32:47]
	v_cvt_pk_bf16_f32 v84, v72, v73
	v_cvt_pk_bf16_f32 v85, v74, v75
	v_cvt_pk_bf16_f32 v86, v76, v77
	v_cvt_pk_bf16_f32 v87, v78, v79
	s_cmp_eq_u32 s27, 0
	s_cbranch_scc1 .Lm_nod_lp
	s_cmp_lt_u32 s28, 9
	s_cbranch_scc0 .Lm_nod_lp
	s_mov_b32 m0, s34
	s_nop 0
	global_load_lds_dwordx4 v2, s[50:51]
	s_mov_b32 m0, s35
	s_nop 0
	global_load_lds_dwordx4 v2, s[52:53]
	s_cmp_lt_u32 s18, 6
	s_cbranch_scc0 .Lm_nod_lp
	s_mov_b32 m0, s36
	s_nop 0
	global_load_lds_dwordx4 v2, s[54:55]
.Lm_nod_lp:
	s_waitcnt lgkmcnt(4)
	v_mfma_f32_32x32x16_f16 v[64:79], v[92:95], v[8:11], 0
	ds_read_b128 v[88:91], v128 offset:28672
	ds_read_b128 v[112:115], v128 offset:12288
	ds_read_b128 v[120:123], v128 offset:14336
	v_exp_f32_e32 v48, v48
	v_exp_f32_e32 v49, v49
	v_exp_f32_e32 v50, v50
	v_exp_f32_e32 v51, v51
	v_mfma_f32_32x32x16_bf16 v[16:31], v[116:119], v[84:87], v[16:31]
	v_exp_f32_e32 v52, v52
	v_exp_f32_e32 v53, v53
	v_exp_f32_e32 v54, v54
	v_exp_f32_e32 v55, v55
	v_mfma_f32_32x32x16_bf16 v[32:47], v[124:127], v[84:87], v[32:47]
	v_cvt_pk_bf16_f32 v80, v48, v49
	v_cvt_pk_bf16_f32 v81, v50, v51
	v_cvt_pk_bf16_f32 v82, v52, v53
	v_cvt_pk_bf16_f32 v83, v54, v55
	ds_read_b128 v[116:119], v128 offset:13312
	ds_read_b128 v[124:127], v128 offset:15360
	v_exp_f32_e32 v56, v56
	v_exp_f32_e32 v57, v57
	v_exp_f32_e32 v58, v58
	v_exp_f32_e32 v59, v59
	s_waitcnt lgkmcnt(7)
	v_mfma_f32_32x32x16_bf16 v[16:31], v[96:99], v[80:83], v[16:31]
	v_exp_f32_e32 v60, v60
	v_exp_f32_e32 v61, v61
	v_exp_f32_e32 v62, v62
	v_exp_f32_e32 v63, v63
	v_mfma_f32_32x32x16_bf16 v[32:47], v[104:107], v[80:83], v[32:47]
	v_cvt_pk_bf16_f32 v84, v56, v57
	v_cvt_pk_bf16_f32 v85, v58, v59
	v_cvt_pk_bf16_f32 v86, v60, v61
	v_cvt_pk_bf16_f32 v87, v62, v63
	s_waitcnt lgkmcnt(4)
	v_mfma_f32_32x32x16_f16 v[48:63], v[88:91], v[8:11], 0
	ds_read_b128 v[92:95], v128 offset:29696
	ds_read_b128 v[96:99], v128 offset:16384
	ds_read_b128 v[104:107], v128 offset:18432
	v_exp_f32_e32 v64, v64
	v_exp_f32_e32 v65, v65
	v_exp_f32_e32 v66, v66
	v_exp_f32_e32 v67, v67
	v_mfma_f32_32x32x16_bf16 v[16:31], v[100:103], v[84:87], v[16:31]
	v_exp_f32_e32 v68, v68
	v_exp_f32_e32 v69, v69
	v_exp_f32_e32 v70, v70
	v_exp_f32_e32 v71, v71
	v_mfma_f32_32x32x16_bf16 v[32:47], v[108:111], v[84:87], v[32:47]
	v_cvt_pk_bf16_f32 v80, v64, v65
	v_cvt_pk_bf16_f32 v81, v66, v67
	v_cvt_pk_bf16_f32 v82, v68, v69
	v_cvt_pk_bf16_f32 v83, v70, v71
	ds_read_b128 v[100:103], v128 offset:17408
	ds_read_b128 v[108:111], v128 offset:19456
	v_exp_f32_e32 v72, v72
	v_exp_f32_e32 v73, v73
	v_exp_f32_e32 v74, v74
	v_exp_f32_e32 v75, v75
	s_waitcnt lgkmcnt(7)
	v_mfma_f32_32x32x16_bf16 v[16:31], v[112:115], v[80:83], v[16:31]
	v_exp_f32_e32 v76, v76
	v_exp_f32_e32 v77, v77
	v_exp_f32_e32 v78, v78
	v_exp_f32_e32 v79, v79
	v_mfma_f32_32x32x16_bf16 v[32:47], v[120:123], v[80:83], v[32:47]
	v_cvt_pk_bf16_f32 v84, v72, v73
	v_cvt_pk_bf16_f32 v85, v74, v75
	v_cvt_pk_bf16_f32 v86, v76, v77
	v_cvt_pk_bf16_f32 v87, v78, v79
	s_waitcnt lgkmcnt(4)
	v_mfma_f32_32x32x16_f16 v[64:79], v[92:95], v[8:11], 0
	ds_read_b128 v[88:91], v129 offset:24576
	ds_read_b128 v[112:115], v128 offset:20480
	ds_read_b128 v[120:123], v128 offset:22528
	v_exp_f32_e32 v48, v48
	v_exp_f32_e32 v49, v49
	v_exp_f32_e32 v50, v50
	v_exp_f32_e32 v51, v51
	v_mfma_f32_32x32x16_bf16 v[16:31], v[116:119], v[84:87], v[16:31]
	v_exp_f32_e32 v52, v52
	v_exp_f32_e32 v53, v53
	v_exp_f32_e32 v54, v54
	v_exp_f32_e32 v55, v55
	v_mfma_f32_32x32x16_bf16 v[32:47], v[124:127], v[84:87], v[32:47]
	v_cvt_pk_bf16_f32 v80, v48, v49
	v_cvt_pk_bf16_f32 v81, v50, v51
	v_cvt_pk_bf16_f32 v82, v52, v53
	v_cvt_pk_bf16_f32 v83, v54, v55
	ds_read_b128 v[116:119], v128 offset:21504
	ds_read_b128 v[124:127], v128 offset:23552
	v_exp_f32_e32 v56, v56
	v_exp_f32_e32 v57, v57
	v_exp_f32_e32 v58, v58
	v_exp_f32_e32 v59, v59
	s_waitcnt lgkmcnt(7)
	v_mfma_f32_32x32x16_bf16 v[16:31], v[96:99], v[80:83], v[16:31]
	v_exp_f32_e32 v60, v60
	v_exp_f32_e32 v61, v61
	v_exp_f32_e32 v62, v62
	v_exp_f32_e32 v63, v63
	v_mfma_f32_32x32x16_bf16 v[32:47], v[104:107], v[80:83], v[32:47]
	v_cvt_pk_bf16_f32 v84, v56, v57
	v_cvt_pk_bf16_f32 v85, v58, v59
	v_cvt_pk_bf16_f32 v86, v60, v61
	v_cvt_pk_bf16_f32 v87, v62, v63
	s_waitcnt lgkmcnt(4)
	v_mfma_f32_32x32x16_f16 v[48:63], v[88:91], v[8:11], 0
	ds_read_b128 v[92:95], v129 offset:25600
	ds_read_b128 v[96:99], v129 offset:0
	ds_read_b128 v[104:107], v129 offset:2048
	v_exp_f32_e32 v64, v64
	v_exp_f32_e32 v65, v65
	v_exp_f32_e32 v66, v66
	v_exp_f32_e32 v67, v67
	v_mfma_f32_32x32x16_bf16 v[16:31], v[100:103], v[84:87], v[16:31]
	v_exp_f32_e32 v68, v68
	v_exp_f32_e32 v69, v69
	v_exp_f32_e32 v70, v70
	v_exp_f32_e32 v71, v71
	v_mfma_f32_32x32x16_bf16 v[32:47], v[108:111], v[84:87], v[32:47]
	v_cvt_pk_bf16_f32 v80, v64, v65
	v_cvt_pk_bf16_f32 v81, v66, v67
	v_cvt_pk_bf16_f32 v82, v68, v69
	v_cvt_pk_bf16_f32 v83, v70, v71
	ds_read_b128 v[100:103], v129 offset:1024
	ds_read_b128 v[108:111], v129 offset:3072
	v_exp_f32_e32 v72, v72
	v_exp_f32_e32 v73, v73
	v_exp_f32_e32 v74, v74
	v_exp_f32_e32 v75, v75
	s_waitcnt lgkmcnt(7)
	v_mfma_f32_32x32x16_bf16 v[16:31], v[112:115], v[80:83], v[16:31]
	v_exp_f32_e32 v76, v76
	v_exp_f32_e32 v77, v77
	v_exp_f32_e32 v78, v78
	v_exp_f32_e32 v79, v79
	v_mfma_f32_32x32x16_bf16 v[32:47], v[120:123], v[80:83], v[32:47]
	v_cvt_pk_bf16_f32 v84, v72, v73
	v_cvt_pk_bf16_f32 v85, v74, v75
	v_cvt_pk_bf16_f32 v86, v76, v77
	v_cvt_pk_bf16_f32 v87, v78, v79
	s_waitcnt lgkmcnt(5)
	s_nop 0
	v_mfma_f32_32x32x16_bf16 v[16:31], v[116:119], v[84:87], v[16:31]
	v_mfma_f32_32x32x16_bf16 v[32:47], v[124:127], v[84:87], v[32:47]
	s_mov_b32 s30, s46
	s_mov_b32 s46, s47
	s_mov_b32 s47, s48
	s_mov_b32 s48, s30
	s_add_u32 s27, s27, 1
	s_cmp_lt_u32 s27, 9
	s_cbranch_scc0 .Lm_flush
	s_cmp_eq_u32 s27, s25
	s_cbranch_scc1 .Lm_flush
	s_waitcnt vmcnt(0)
